# speedup vs baseline: 1.0504x; 1.0273x over previous
_Z5k_aggILi0EEvPKDF16_S1_S1_PK15HIP_vector_typeIiLj4EEPKiS7_PKfS1_S9_PfPDF16_S1_S9_SB_SB_:
	s_lshr_b32 s3, s2, 3
	s_bitcmp1_b32 s3, 3
	s_cbranch_scc0 .Lnosleep_a0_0
	s_sleep 127
	s_sleep 23
.Lnosleep_a0_0:
	s_load_dwordx2 s[6:7], s[0:1], 0x30
	s_load_dwordx2 s[4:5], s[0:1], 0x18
	s_load_dwordx4 s[24:27], s[0:1], 0x20
	s_load_dwordx2 s[30:31], s[0:1], 0x10
	s_load_dwordx4 s[20:23], s[0:1], 0x0
	s_load_dwordx4 s[16:19], s[0:1], 0x58
	s_load_dwordx2 s[28:29], s[0:1], 0x40
	s_and_b32 s36, s2, 7
	s_lshr_b32 s37, s2, 3
	s_mul_i32 s38, s36, 0x61
	s_min_u32 s36, s36, 6
	s_add_i32 s40, s36, s37
	s_add_i32 s40, s40, s38
	s_lshl_b32 s33, s40, 6
	v_lshrrev_b32_e32 v100, 3, v0
	v_and_b32_e32 v101, 7, v0
	v_or_b32_e32 v102, s33, v100
	v_mov_b32_e32 v103, 0
	v_and_b32_e32 v1, 63, v0
	v_lshlrev_b32_e32 v2, 2, v1
	v_or_b32_e32 v16, 0x300, v1
	v_lshlrev_b32_e32 v104, 5, v102
	v_lshl_or_b32 v104, v101, 2, v104
	s_waitcnt lgkmcnt(0)
	v_lshl_add_u64 v[106:107], v[102:103], 4, s[4:5]
	global_load_dwordx3 v[42:44], v[106:107], off
	global_load_dwordx3 v[46:48], v[106:107], off offset:512
	global_load_dword v45, v104, s[26:27]
	global_load_dword v49, v104, s[26:27] offset:1024
	global_load_dword v4, v2, s[6:7]
	global_load_dword v5, v2, s[6:7] offset:256
	global_load_dword v6, v2, s[6:7] offset:512
	global_load_dword v7, v2, s[6:7] offset:768
	global_load_dword v8, v2, s[6:7] offset:1024
	global_load_dword v9, v2, s[6:7] offset:1280
	global_load_dword v10, v2, s[6:7] offset:1536
	global_load_dword v11, v2, s[6:7] offset:1792
	global_load_dword v12, v2, s[6:7] offset:2048
	global_load_dword v13, v2, s[6:7] offset:2304
	global_load_dword v14, v2, s[6:7] offset:2560
	global_load_dword v15, v2, s[6:7] offset:2816
	s_movk_i32 s3, 0x30e
	v_mov_b32_e32 v3, 0
	v_cmp_gt_u32_e32 vcc, s3, v16
	s_waitcnt vmcnt(11)
	v_add_f32_e32 v1, 0, v4
	s_waitcnt vmcnt(10)
	v_add_f32_e32 v1, v1, v5
	s_waitcnt vmcnt(9)
	v_add_f32_e32 v1, v1, v6
	s_waitcnt vmcnt(8)
	v_add_f32_e32 v1, v1, v7
	s_waitcnt vmcnt(7)
	v_add_f32_e32 v1, v1, v8
	s_waitcnt vmcnt(6)
	v_add_f32_e32 v1, v1, v9
	s_waitcnt vmcnt(5)
	v_add_f32_e32 v1, v1, v10
	s_waitcnt vmcnt(4)
	v_add_f32_e32 v1, v1, v11
	s_waitcnt vmcnt(3)
	v_add_f32_e32 v1, v1, v12
	s_waitcnt vmcnt(2)
	v_add_f32_e32 v1, v1, v13
	s_waitcnt vmcnt(1)
	v_add_f32_e32 v1, v1, v14
	s_waitcnt vmcnt(0)
	v_add_f32_e32 v1, v1, v15
	s_and_saveexec_b64 s[8:9], vcc
	s_cbranch_execz .LBB2_2
	v_lshl_add_u64 v[4:5], s[6:7], 0, v[2:3]
	global_load_dword v2, v[4:5], off offset:3072
	s_waitcnt vmcnt(0)
	v_add_f32_e32 v1, v1, v2

.Lpl_last_a0:
	s_waitcnt vmcnt(6)
	s_mov_b64 exec, s[44:45]
	v_pk_minimum3_f16 v52, v52, v10, v14
	v_pk_maximum3_f16 v100, v100, v10, v14
	v_pk_minimum3_f16 v99, v99, v11, v15
	v_pk_maximum3_f16 v101, v101, v11, v15
	v_pk_minimum3_f16 v98, v98, v12, v16
	v_pk_maximum3_f16 v105, v105, v12, v16
	v_pk_minimum3_f16 v103, v103, v13, v17
	v_pk_maximum3_f16 v104, v104, v13, v17
	v_pk_mul_f16 v110, v10, v10
	v_mov_b32_e32 v106, v10
	v_pk_mul_f16 v111, v11, v11
	v_mov_b32_e32 v107, v11
	v_pk_mul_f16 v112, v12, v12
	v_mov_b32_e32 v108, v12
	v_pk_mul_f16 v113, v13, v13
	v_mov_b32_e32 v109, v13
	s_mov_b64 exec, s[46:47]
	v_pk_add_f16 v106, v106, v14
	v_pk_fma_f16 v110, v14, v14, v110
	v_pk_add_f16 v107, v107, v15
	v_pk_fma_f16 v111, v15, v15, v111
	v_pk_add_f16 v108, v108, v16
	v_pk_fma_f16 v112, v16, v16, v112
	v_pk_add_f16 v109, v109, v17
	v_pk_fma_f16 v113, v17, v17, v113
	s_mov_b64 exec, -1
	s_waitcnt vmcnt(4)
	s_mov_b64 exec, s[48:49]
	v_pk_minimum3_f16 v52, v52, v18, v22
	v_pk_maximum3_f16 v100, v100, v18, v22
	v_pk_minimum3_f16 v99, v99, v19, v23
	v_pk_maximum3_f16 v101, v101, v19, v23
	v_pk_minimum3_f16 v98, v98, v20, v24
	v_pk_maximum3_f16 v105, v105, v20, v24
	v_pk_minimum3_f16 v103, v103, v21, v25
	v_pk_maximum3_f16 v104, v104, v21, v25
	v_pk_add_f16 v106, v106, v18
	v_pk_fma_f16 v110, v18, v18, v110
	v_pk_add_f16 v107, v107, v19
	v_pk_fma_f16 v111, v19, v19, v111
	v_pk_add_f16 v108, v108, v20
	v_pk_fma_f16 v112, v20, v20, v112
	v_pk_add_f16 v109, v109, v21
	v_pk_fma_f16 v113, v21, v21, v113
	s_mov_b64 exec, s[50:51]
	v_pk_add_f16 v106, v106, v22
	v_pk_fma_f16 v110, v22, v22, v110
	v_pk_add_f16 v107, v107, v23
	v_pk_fma_f16 v111, v23, v23, v111
	v_pk_add_f16 v108, v108, v24
	v_pk_fma_f16 v112, v24, v24, v112
	v_pk_add_f16 v109, v109, v25
	v_pk_fma_f16 v113, v25, v25, v113
	s_mov_b64 exec, -1
	s_waitcnt vmcnt(2)
	s_mov_b64 exec, s[52:53]
	v_pk_minimum3_f16 v52, v52, v26, v30
	v_pk_maximum3_f16 v100, v100, v26, v30
	v_pk_minimum3_f16 v99, v99, v27, v31
	v_pk_maximum3_f16 v101, v101, v27, v31
	v_pk_minimum3_f16 v98, v98, v28, v32
	v_pk_maximum3_f16 v105, v105, v28, v32
	v_pk_minimum3_f16 v103, v103, v29, v33
	v_pk_maximum3_f16 v104, v104, v29, v33
	v_pk_add_f16 v106, v106, v26
	v_pk_fma_f16 v110, v26, v26, v110
	v_pk_add_f16 v107, v107, v27
	v_pk_fma_f16 v111, v27, v27, v111
	v_pk_add_f16 v108, v108, v28
	v_pk_fma_f16 v112, v28, v28, v112
	v_pk_add_f16 v109, v109, v29
	v_pk_fma_f16 v113, v29, v29, v113
	s_mov_b64 exec, s[54:55]
	v_pk_add_f16 v106, v106, v30
	v_pk_fma_f16 v110, v30, v30, v110
	v_pk_add_f16 v107, v107, v31
	v_pk_fma_f16 v111, v31, v31, v111
	v_pk_add_f16 v108, v108, v32
	v_pk_fma_f16 v112, v32, v32, v112
	v_pk_add_f16 v109, v109, v33
	v_pk_fma_f16 v113, v33, v33, v113
	s_mov_b64 exec, -1
	s_waitcnt vmcnt(0)
	s_mov_b64 exec, s[56:57]
	v_pk_minimum3_f16 v52, v52, v34, v38
	v_pk_maximum3_f16 v100, v100, v34, v38
	v_pk_minimum3_f16 v99, v99, v35, v39
	v_pk_maximum3_f16 v101, v101, v35, v39
	v_pk_minimum3_f16 v98, v98, v36, v40
	v_pk_maximum3_f16 v105, v105, v36, v40
	v_pk_minimum3_f16 v103, v103, v37, v41
	v_pk_maximum3_f16 v104, v104, v37, v41
	v_pk_add_f16 v106, v106, v34
	v_pk_fma_f16 v110, v34, v34, v110
	v_pk_add_f16 v107, v107, v35
	v_pk_fma_f16 v111, v35, v35, v111
	v_pk_add_f16 v108, v108, v36
	v_pk_fma_f16 v112, v36, v36, v112
	v_pk_add_f16 v109, v109, v37
	v_pk_fma_f16 v113, v37, v37, v113
	s_mov_b64 exec, s[58:59]
	v_pk_add_f16 v106, v106, v38
	v_pk_fma_f16 v110, v38, v38, v110
	v_pk_add_f16 v107, v107, v39
	v_pk_fma_f16 v111, v39, v39, v111
	v_pk_add_f16 v108, v108, v40
	v_pk_fma_f16 v112, v40, v40, v112
	v_pk_add_f16 v109, v109, v41
	v_pk_fma_f16 v113, v41, v41, v113
	s_mov_b64 exec, -1
	s_mov_b64 exec, s[44:45]
	v_cvt_f32_f16_e32 v114, v106
	v_cvt_f32_f16_sdwa v115, v106 dst_sel:DWORD dst_unused:UNUSED_PAD src0_sel:WORD_1
	v_cvt_f32_f16_e32 v118, v110
	v_cvt_f32_f16_sdwa v119, v110 dst_sel:DWORD dst_unused:UNUSED_PAD src0_sel:WORD_1
	v_pk_add_f32 v[72:73], v[72:73], v[114:115]
	v_cvt_f32_f16_e32 v114, v107
	v_cvt_f32_f16_sdwa v115, v107 dst_sel:DWORD dst_unused:UNUSED_PAD src0_sel:WORD_1
	v_pk_add_f32 v[76:77], v[76:77], v[118:119]
	v_cvt_f32_f16_e32 v118, v111
	v_cvt_f32_f16_sdwa v119, v111 dst_sel:DWORD dst_unused:UNUSED_PAD src0_sel:WORD_1
	v_pk_add_f32 v[70:71], v[70:71], v[114:115]
	v_cvt_f32_f16_e32 v114, v108
	v_cvt_f32_f16_sdwa v115, v108 dst_sel:DWORD dst_unused:UNUSED_PAD src0_sel:WORD_1
	v_pk_add_f32 v[74:75], v[74:75], v[118:119]
	v_cvt_f32_f16_e32 v118, v112
	v_cvt_f32_f16_sdwa v119, v112 dst_sel:DWORD dst_unused:UNUSED_PAD src0_sel:WORD_1
	v_pk_add_f32 v[64:65], v[64:65], v[114:115]
	v_cvt_f32_f16_e32 v114, v109
	v_cvt_f32_f16_sdwa v115, v109 dst_sel:DWORD dst_unused:UNUSED_PAD src0_sel:WORD_1
	v_pk_add_f32 v[68:69], v[68:69], v[118:119]
	v_cvt_f32_f16_e32 v118, v113
	v_cvt_f32_f16_sdwa v119, v113 dst_sel:DWORD dst_unused:UNUSED_PAD src0_sel:WORD_1
	v_pk_add_f32 v[62:63], v[62:63], v[114:115]
	s_nop 0
	v_pk_add_f32 v[66:67], v[66:67], v[118:119]
	s_mov_b64 exec, -1
	s_waitcnt vmcnt(0)
	s_cmp_eq_u64 s[4:5], 0
	s_cbranch_scc0 .Lnowp_a0
	v_readfirstlane_b32 s60, v0
	v_and_b32_e32 v79, 63, v0
	s_nop 3
	s_lshr_b32 s60, s60, 6
	s_mul_i32 s60, s60, 0x6800
	s_add_u32 s62, s34, s60
	s_addc_u32 s63, s35, 0
	v_lshlrev_b32_e32 v79, 4, v79
	global_load_dwordx4 v[88:91], v79, s[62:63]
	global_load_dwordx4 v[106:109], v79, s[62:63] offset:1024
	global_load_dwordx4 v[110:113], v79, s[62:63] offset:2048
	global_load_dwordx4 v[114:117], v79, s[62:63] offset:3072
.Lnowp_a0:
	s_xor_b64 s[0:1], s[4:5], -1
	s_and_saveexec_b64 s[4:5], s[6:7]
	s_xor_b64 s[4:5], exec, s[4:5]
	s_cbranch_execz .LBB2_22
	v_cndmask_b32_e64 v6, 0, v95, s[2:3]
	v_pack_b32_f16 v13, v6, v6
	v_mov_b32_e32 v12, v13
	s_waitcnt lgkmcnt(0)
	v_mov_b32_e32 v11, v13
	v_mov_b32_e32 v10, v13
.LBB2_22:
	s_or_saveexec_b64 s[2:3], s[4:5]
	v_mov_b32_e32 v18, 0
	v_mov_b32_e32 v19, 0
	v_mov_b32_e32 v20, 0
	v_mov_b32_e32 v21, 0
	v_mov_b32_e32 v22, 0
	v_mov_b32_e32 v23, 0
	v_mov_b32_e32 v24, 0
	v_mov_b32_e32 v25, 0
	v_mov_b32_e32 v14, 0
	v_mov_b32_e32 v15, 0
	v_mov_b32_e32 v16, 0
	v_mov_b32_e32 v17, 0
	s_xor_b64 exec, exec, s[2:3]
	s_cbranch_execz .LBB2_24
	v_cvt_f32_u32_e32 v10, v97
	v_mov_b32_e32 v14, v76
	v_cvt_f32_f16_sdwa v13, v6 dst_sel:DWORD dst_unused:UNUSED_PAD src0_sel:WORD_1
	v_cvt_f32_f16_e32 v12, v6
	v_rcp_iflag_f32_e32 v10, v10
	v_mov_b32_e32 v18, v74
	v_pk_add_f16 v22, v6, v52
	v_pk_add_f16 v23, v7, v99
	s_waitcnt lgkmcnt(0)
	v_pk_mul_f32 v[16:17], v[10:11], v[72:73] op_sel_hi:[0,1]
	v_mov_b32_e32 v11, v16
	v_mov_b32_e32 v15, v16
	v_pk_mul_f32 v[14:15], v[10:11], v[14:15]
	v_mov_b32_e32 v16, v77
	v_sub_f32_e32 v14, v14, v15
	v_max_f32_e32 v14, 0, v14
	v_mov_b32_e32 v11, v17
	v_add_f32_e32 v14, 0x3727c5ac, v14
	v_sqrt_f32_e32 v26, v14
	v_pk_mul_f32 v[14:15], v[10:11], v[16:17]
	v_pk_add_f16 v24, v8, v98
	v_sub_f32_e32 v11, v14, v15
	v_max_f32_e32 v11, 0, v11
	v_pk_fma_f32 v[12:13], v[10:11], v[72:73], v[12:13] op_sel_hi:[0,1,1]
	v_add_f32_e32 v11, 0x3727c5ac, v11
	v_pk_mul_f32 v[16:17], v[10:11], v[70:71] op_sel_hi:[0,1]
	v_sqrt_f32_e32 v27, v11
	v_mov_b32_e32 v11, v16
	v_mov_b32_e32 v19, v16
	v_pk_mul_f32 v[18:19], v[10:11], v[18:19]
	v_cvt_pk_f16_f32 v14, v12, v13
	v_sub_f32_e32 v11, v18, v19
	v_max_f32_e32 v11, 0, v11
	v_add_f32_e32 v11, 0x3727c5ac, v11
	v_cvt_f32_f16_sdwa v13, v7 dst_sel:DWORD dst_unused:UNUSED_PAD src0_sel:WORD_1
	v_cvt_f32_f16_e32 v12, v7
	v_sqrt_f32_e32 v28, v11
	v_mov_b32_e32 v11, v17
	v_mov_b32_e32 v16, v75
	v_pk_mul_f32 v[16:17], v[10:11], v[16:17]
	v_mov_b32_e32 v18, v68
	v_sub_f32_e32 v11, v16, v17
	v_max_f32_e32 v11, 0, v11
	v_pk_fma_f32 v[12:13], v[10:11], v[70:71], v[12:13] op_sel_hi:[0,1,1]
	v_add_f32_e32 v11, 0x3727c5ac, v11
	v_pk_mul_f32 v[16:17], v[10:11], v[64:65] op_sel_hi:[0,1]
	v_sqrt_f32_e32 v29, v11
	v_mov_b32_e32 v11, v16
	v_mov_b32_e32 v19, v16
	v_pk_mul_f32 v[18:19], v[10:11], v[18:19]
	v_cvt_pk_f16_f32 v15, v12, v13
	v_sub_f32_e32 v11, v18, v19
	v_max_f32_e32 v11, 0, v11
	v_add_f32_e32 v11, 0x3727c5ac, v11
	v_cvt_f32_f16_sdwa v13, v8 dst_sel:DWORD dst_unused:UNUSED_PAD src0_sel:WORD_1
	v_cvt_f32_f16_e32 v12, v8
	v_sqrt_f32_e32 v30, v11
	v_mov_b32_e32 v11, v17
	v_mov_b32_e32 v16, v69
	v_pk_mul_f32 v[16:17], v[10:11], v[16:17]
	v_cvt_f32_f16_sdwa v19, v9 dst_sel:DWORD dst_unused:UNUSED_PAD src0_sel:WORD_1
	v_sub_f32_e32 v11, v16, v17
	v_max_f32_e32 v11, 0, v11
	v_pk_fma_f32 v[12:13], v[10:11], v[64:65], v[12:13] op_sel_hi:[0,1,1]
	v_cvt_pk_f16_f32 v16, v12, v13
	v_add_f32_e32 v11, 0x3727c5ac, v11
	v_mov_b32_e32 v12, v66
	v_mov_b32_e32 v13, v62
	v_pk_mul_f32 v[12:13], v[10:11], v[12:13] op_sel_hi:[0,1]
	v_sqrt_f32_e32 v31, v11
	v_fma_f32 v11, -v13, v13, v12
	v_max_f32_e32 v11, 0, v11
	v_add_f32_e32 v11, 0x3727c5ac, v11
	v_mov_b32_e32 v62, v67
	v_cvt_f32_f16_e32 v18, v9
	v_sqrt_f32_e32 v32, v11
	v_pk_mul_f32 v[10:11], v[10:11], v[62:63] op_sel_hi:[0,1]
	v_fma_f32 v10, -v11, v11, v10
	v_max_f32_e32 v12, 0, v10
	v_mov_b32_e32 v10, v13
	v_pk_add_f32 v[10:11], v[10:11], v[18:19]
	v_pk_add_f16 v18, v6, v100
	v_cvt_pk_f16_f32 v17, v10, v11
	v_add_f32_e32 v10, 0x3727c5ac, v12
	v_sqrt_f32_e32 v13, v10
	v_pk_add_f16 v19, v7, v101
	v_pk_add_f16 v20, v8, v105
	v_pk_add_f16 v25, v9, v103
	v_pk_add_f16 v21, v9, v104
	v_cvt_pk_f16_f32 v10, v26, v27
	v_cvt_pk_f16_f32 v11, v28, v29
	v_cvt_pk_f16_f32 v12, v30, v31
	v_cvt_pk_f16_f32 v13, v32, v13
.LBB2_24:
	s_or_b64 exec, exec, s[2:3]
	s_and_saveexec_b64 s[2:3], vcc
	s_cbranch_execz .LBB2_26
	v_lshl_add_u32 v6, v96, 7, v57
	ds_write_b128 v6, v[2:5]
.LBB2_26:
	s_or_b64 exec, exec, s[2:3]
	v_lshlrev_b32_e32 v2, 9, v96
	v_or_b32_e32 v3, v2, v83
	ds_write_b128 v3, v[14:17]
	v_or_b32_e32 v3, v2, v84
	ds_write_b128 v3, v[22:25]
	v_or_b32_e32 v3, v2, v85
	v_or_b32_e32 v2, v2, v86
	ds_write_b128 v3, v[18:21]
	s_waitcnt lgkmcnt(0)
	ds_write_b128 v2, v[10:13]
	s_and_saveexec_b64 s[2:3], s[8:9]
	s_cbranch_execz .LBB2_5
	v_cvt_f32_i32_e32 v2, v97
	v_lshlrev_b32_e32 v4, 3, v96
	v_max_f32_e32 v2, 1.0, v2
	v_add_f32_e32 v2, 1.0, v2
	v_log_f32_e32 v2, v2
	s_nop 0
	v_mul_f32_e32 v2, 0x3f317218, v2
	v_rcp_f32_e32 v3, v2
	s_nop 0
	v_pk_mul_f32 v[2:3], v[54:55], v[2:3]
	ds_write_b64 v4, v[2:3] offset:39936
	s_branch .LBB2_5

.LBB2_30:
	s_or_b64 exec, exec, s[2:3]
	v_ashrrev_i32_e32 v86, 6, v74
	v_mul_lo_u32 v4, v86, 26
	v_ashrrev_i32_e32 v5, 31, v4
	v_lshlrev_b64 v[4:5], 10, v[4:5]
	v_lshl_add_u64 v[4:5], s[34:35], 0, v[4:5]
	v_lshlrev_b32_e32 v2, 4, v6
	v_lshl_add_u64 v[82:83], v[4:5], 0, v[2:3]
	s_movk_i32 s2, 0x2000
	v_add_co_u32_e32 v2, vcc, s2, v82
	s_movk_i32 s2, 0x4000
	s_nop 0
	v_addc_co_u32_e32 v3, vcc, 0, v83, vcc
	v_add_co_u32_e32 v4, vcc, s2, v82
	s_movk_i32 s2, 0x1000
	s_nop 0
	v_addc_co_u32_e32 v5, vcc, 0, v83, vcc
	global_load_dwordx4 v[42:45], v[2:3], off offset:2048
	global_load_dwordx4 v[26:29], v[2:3], off offset:3072
	global_load_dwordx4 v[46:49], v[4:5], off offset:2048
	global_load_dwordx4 v[14:17], v[4:5], off offset:3072
	v_add_co_u32_e32 v2, vcc, s2, v82
	s_movk_i32 s2, 0x3000
	s_nop 0
	v_addc_co_u32_e32 v3, vcc, 0, v83, vcc
	v_add_co_u32_e32 v4, vcc, s2, v82
	s_movk_i32 s2, 0x5000
	s_nop 0
	v_addc_co_u32_e32 v5, vcc, 0, v83, vcc
	v_add_co_u32_e32 v6, vcc, s2, v82
	v_mov_b32_e32 v79, 0x8000
	s_nop 0
	v_addc_co_u32_e32 v7, vcc, 0, v83, vcc
	global_load_dwordx4 v[22:25], v[2:3], off
	global_load_dwordx4 v[10:13], v[2:3], off offset:1024
	global_load_dwordx4 v[34:37], v[4:5], off
	s_nop 0
	global_load_dwordx4 v[2:5], v[4:5], off offset:1024
	s_nop 0
	global_load_dwordx4 v[30:33], v[6:7], off
	s_nop 0
	global_load_dwordx4 v[6:9], v[6:7], off offset:1024
	v_bitop3_b32 v66, v74, v1, 7 bitop3:0x6c
	v_lshl_or_b32 v78, v84, 7, v79
	v_lshl_or_b32 v75, v66, 4, v78
	s_waitcnt vmcnt(12)
	v_mov_b32_e32 v62, v88
	v_mov_b32_e32 v63, v89
	v_mov_b32_e32 v64, v90
	v_mov_b32_e32 v65, v91
	v_mov_b32_e32 v58, v106
	v_mov_b32_e32 v59, v107
	v_mov_b32_e32 v60, v108
	v_mov_b32_e32 v61, v109
	v_mov_b32_e32 v38, v110
	v_mov_b32_e32 v39, v111
	v_mov_b32_e32 v40, v112
	v_mov_b32_e32 v41, v113
	v_mov_b32_e32 v18, v114
	v_mov_b32_e32 v19, v115
	v_mov_b32_e32 v20, v116
	v_mov_b32_e32 v21, v117
	s_waitcnt lgkmcnt(0)
	s_barrier
	ds_read_b128 v[66:69], v75
	ds_read_b128 v[70:73], v75 offset:2048
	ds_read_b128 v[88:91], v75 offset:4096
	v_and_b32_e32 v85, 7, v74
	v_or_b32_e32 v80, 48, v84
	v_min_u32_e32 v80, 55, v80
	v_and_b32_e32 v87, 7, v80
	s_waitcnt vmcnt(10) lgkmcnt(2)
	v_mfma_f32_16x16x32_f16 v[66:69], v[66:69], v[62:65], 0
	s_waitcnt lgkmcnt(1)
	v_mfma_f32_16x16x32_f16 v[70:73], v[70:73], v[62:65], 0
	s_waitcnt lgkmcnt(0)
	v_mfma_f32_16x16x32_f16 v[74:77], v[88:91], v[62:65], 0
	v_lshl_or_b32 v88, v80, 7, v79
	s_and_saveexec_b64 s[2:3], s[0:1]
	v_xor_b32_e32 v54, v87, v1
	v_lshl_add_u32 v54, v54, 4, v88
	ds_read_b128 v[54:57], v54
	s_or_b64 exec, exec, s[2:3]
	v_bitop3_b32 v79, v85, v1, 4 bitop3:0x1e
	v_lshl_add_u32 v89, v79, 4, v78
	ds_read_b128 v[90:93], v89
	s_waitcnt lgkmcnt(1)
	v_mfma_f32_16x16x32_f16 v[78:81], v[54:57], v[62:65], 0
	ds_read_b128 v[54:57], v89 offset:2048
	s_waitcnt vmcnt(12) lgkmcnt(0)
	v_mfma_f32_16x16x32_f16 v[62:65], v[54:57], v[58:61], v[70:73]
	ds_read_b128 v[54:57], v89 offset:4096
	s_nop 1
	v_or_b32_e32 v70, 4, v1
	v_mfma_f32_16x16x32_f16 v[66:69], v[90:93], v[58:61], v[66:69]
	s_waitcnt lgkmcnt(0)
	v_mfma_f32_16x16x32_f16 v[54:57], v[54:57], v[58:61], v[74:77]
	s_and_saveexec_b64 s[2:3], s[0:1]
	v_xor_b32_e32 v50, v87, v70
	v_lshl_add_u32 v50, v50, 4, v88
	ds_read_b128 v[50:53], v50
	s_or_b64 exec, exec, s[2:3]
	s_waitcnt lgkmcnt(0)
	v_mfma_f32_16x16x32_f16 v[50:53], v[50:53], v[58:61], v[78:81]
	v_lshlrev_b32_e32 v87, 9, v84
	v_xor_b32_e32 v58, v1, v84
	v_lshl_or_b32 v71, v58, 4, v87
	ds_read_b128 v[58:61], v71
	ds_read_b128 v[72:75], v71 offset:8192
	ds_read_b128 v[92:95], v71 offset:16384
	ds_read_b128 v[96:99], v71 offset:24576
	s_waitcnt vmcnt(11) lgkmcnt(3)
	v_mfma_f32_16x16x32_f16 v[66:69], v[58:61], v[38:41], v[66:69]
	s_cmpk_lt_u32 s40, 0x30c
	s_mov_b64 s[0:1], -1
	s_waitcnt lgkmcnt(2)
	v_mfma_f32_16x16x32_f16 v[62:65], v[72:75], v[38:41], v[62:65]
	s_waitcnt lgkmcnt(1)
	v_mfma_f32_16x16x32_f16 v[54:57], v[92:95], v[38:41], v[54:57]
	s_waitcnt lgkmcnt(0)
	v_mfma_f32_16x16x32_f16 v[38:41], v[96:99], v[38:41], v[50:53]
	s_nop 2
	v_xor_b32_e32 v50, v70, v84
	v_lshl_or_b32 v80, v50, 4, v87
	s_waitcnt vmcnt(9)
	v_mfma_f32_16x16x32_f16 v[76:79], v[58:61], v[42:45], 0
	s_waitcnt vmcnt(7)
	v_mfma_f32_16x16x32_f16 v[58:61], v[58:61], v[46:49], 0
	v_mfma_f32_16x16x32_f16 v[88:91], v[72:75], v[42:45], 0
	v_mfma_f32_16x16x32_f16 v[72:75], v[72:75], v[46:49], 0
	v_mfma_f32_16x16x32_f16 v[100:103], v[92:95], v[42:45], 0
	v_mfma_f32_16x16x32_f16 v[92:95], v[92:95], v[46:49], 0
	v_mfma_f32_16x16x32_f16 v[42:45], v[96:99], v[42:45], 0
	v_mfma_f32_16x16x32_f16 v[46:49], v[96:99], v[46:49], 0
	ds_read_b128 v[50:53], v80
	ds_read_b128 v[96:99], v80 offset:8192
	s_waitcnt lgkmcnt(1)
	v_mfma_f32_16x16x32_f16 v[66:69], v[50:53], v[18:21], v[66:69]
	v_mfma_f32_16x16x32_f16 v[76:79], v[50:53], v[26:29], v[76:79]
	s_waitcnt vmcnt(6)
	v_mfma_f32_16x16x32_f16 v[50:53], v[50:53], v[14:17], v[58:61]
	s_waitcnt lgkmcnt(0)
	v_mfma_f32_16x16x32_f16 v[58:61], v[96:99], v[18:21], v[62:65]
	v_mfma_f32_16x16x32_f16 v[62:65], v[96:99], v[26:29], v[88:91]
	v_mfma_f32_16x16x32_f16 v[70:73], v[96:99], v[14:17], v[72:75]
	s_nop 1
	ds_read_b128 v[88:91], v80 offset:16384
	ds_read_b128 v[96:99], v80 offset:24576
	s_waitcnt lgkmcnt(1)
	v_mfma_f32_16x16x32_f16 v[54:57], v[88:91], v[18:21], v[54:57]
	s_waitcnt lgkmcnt(0)
	v_mfma_f32_16x16x32_f16 v[18:21], v[96:99], v[18:21], v[38:41]
	s_nop 2
	v_bitop3_b32 v38, v1, v84, 8 bitop3:0x36
	v_lshl_or_b32 v74, v38, 4, v87
	v_mfma_f32_16x16x32_f16 v[100:103], v[88:91], v[26:29], v[100:103]
	v_mfma_f32_16x16x32_f16 v[26:29], v[96:99], v[26:29], v[42:45]
	ds_read_b128 v[38:41], v74
	s_nop 1
	ds_read_b128 v[42:45], v74 offset:8192
	v_mfma_f32_16x16x32_f16 v[88:91], v[88:91], v[14:17], v[92:95]
	v_mfma_f32_16x16x32_f16 v[14:17], v[96:99], v[14:17], v[46:49]
	s_waitcnt vmcnt(5) lgkmcnt(1)
	v_mfma_f32_16x16x32_f16 v[46:49], v[38:41], v[22:25], v[66:69]
	s_waitcnt vmcnt(3)
	v_mfma_f32_16x16x32_f16 v[66:69], v[38:41], v[34:37], v[76:79]
	s_waitcnt vmcnt(1)
	v_mfma_f32_16x16x32_f16 v[38:41], v[38:41], v[30:33], v[50:53]
	s_nop 0
	v_add_co_u32_e32 v78, vcc, 0x1000, v82
	s_waitcnt lgkmcnt(0)
	v_mfma_f32_16x16x32_f16 v[50:53], v[42:45], v[22:25], v[58:61]
	v_addc_co_u32_e32 v79, vcc, 0, v83, vcc
	v_add_co_u32_e32 v80, vcc, 0x3000, v82
	v_mfma_f32_16x16x32_f16 v[58:61], v[42:45], v[34:37], v[62:65]
	v_mfma_f32_16x16x32_f16 v[42:45], v[42:45], v[30:33], v[70:73]
	s_nop 1
	ds_read_b128 v[62:65], v74 offset:16384
	ds_read_b128 v[70:73], v74 offset:24576
	s_waitcnt lgkmcnt(1)
	v_mfma_f32_16x16x32_f16 v[54:57], v[62:65], v[22:25], v[54:57]
	s_waitcnt lgkmcnt(0)
	v_mfma_f32_16x16x32_f16 v[18:21], v[70:73], v[22:25], v[18:21]
	v_mfma_f32_16x16x32_f16 v[22:25], v[70:73], v[34:37], v[26:29]
	s_nop 2
	v_bitop3_b32 v26, v1, v84, 12 bitop3:0x36
	v_lshl_or_b32 v81, v26, 4, v87
	v_mfma_f32_16x16x32_f16 v[74:77], v[62:65], v[34:37], v[100:103]
	v_mfma_f32_16x16x32_f16 v[62:65], v[62:65], v[30:33], v[88:91]
	v_mfma_f32_16x16x32_f16 v[14:17], v[70:73], v[30:33], v[14:17]
	ds_read_b128 v[26:29], v81
	ds_read_b128 v[30:33], v81 offset:8192
	s_waitcnt lgkmcnt(1)
	v_mfma_f32_16x16x32_f16 v[34:37], v[26:29], v[10:13], v[46:49]
	v_mfma_f32_16x16x32_f16 v[46:49], v[26:29], v[2:5], v[66:69]
	s_waitcnt vmcnt(0)
	v_mfma_f32_16x16x32_f16 v[26:29], v[26:29], v[6:9], v[38:41]
	s_nop 0
	global_load_dwordx4 v[66:69], v[78:79], off offset:2048
	s_waitcnt lgkmcnt(0)
	v_mfma_f32_16x16x32_f16 v[38:41], v[30:33], v[10:13], v[50:53]
	s_nop 2
	ds_read_b128 v[50:53], v81 offset:16384
	v_mfma_f32_16x16x32_f16 v[58:61], v[30:33], v[2:5], v[58:61]
	v_mfma_f32_16x16x32_f16 v[30:33], v[30:33], v[6:9], v[42:45]
	s_nop 2
	ds_read_b128 v[42:45], v81 offset:24576
	v_addc_co_u32_e32 v81, vcc, 0, v83, vcc
	v_add_co_u32_e32 v88, vcc, 0x5000, v82
	s_waitcnt lgkmcnt(1)
	v_mfma_f32_16x16x32_f16 v[54:57], v[50:53], v[10:13], v[54:57]
	v_addc_co_u32_e32 v89, vcc, 0, v83, vcc
	v_mfma_f32_16x16x32_f16 v[70:73], v[50:53], v[2:5], v[74:77]
	s_nop 2
	global_load_dwordx4 v[74:77], v[80:81], off offset:2048
	s_waitcnt lgkmcnt(0)
	v_mfma_f32_16x16x32_f16 v[10:13], v[42:45], v[10:13], v[18:21]
	s_nop 2
	global_load_dwordx4 v[18:21], v[88:89], off offset:2048
	v_mfma_f32_16x16x32_f16 v[50:53], v[50:53], v[6:9], v[62:65]
	s_nop 2
	v_bitop3_b32 v62, v1, v84, 16 bitop3:0x36
	v_lshl_or_b32 v90, v62, 4, v87
	v_mfma_f32_16x16x32_f16 v[2:5], v[42:45], v[2:5], v[22:25]
	global_load_dwordx4 v[62:65], v[80:81], off offset:3072
	v_mfma_f32_16x16x32_f16 v[6:9], v[42:45], v[6:9], v[14:17]
	global_load_dwordx4 v[42:45], v[78:79], off offset:3072
	ds_read_b128 v[22:25], v90
	global_load_dwordx4 v[78:81], v[88:89], off offset:3072
	ds_read_b128 v[14:17], v90 offset:8192
	s_waitcnt vmcnt(5) lgkmcnt(1)
	v_mfma_f32_16x16x32_f16 v[34:37], v[22:25], v[66:69], v[34:37]
	s_waitcnt vmcnt(4)
	v_mfma_f32_16x16x32_f16 v[46:49], v[22:25], v[74:77], v[46:49]
	s_waitcnt vmcnt(3)
	v_mfma_f32_16x16x32_f16 v[22:25], v[22:25], v[18:21], v[26:29]
	s_waitcnt lgkmcnt(0)
	v_mfma_f32_16x16x32_f16 v[26:29], v[14:17], v[66:69], v[38:41]
	v_mfma_f32_16x16x32_f16 v[38:41], v[14:17], v[74:77], v[58:61]
	v_mfma_f32_16x16x32_f16 v[14:17], v[14:17], v[18:21], v[30:33]
	s_nop 2
	ds_read_b128 v[30:33], v90 offset:16384
	ds_read_b128 v[58:61], v90 offset:24576
	s_waitcnt lgkmcnt(1)
	v_mfma_f32_16x16x32_f16 v[54:57], v[30:33], v[66:69], v[54:57]
	v_mfma_f32_16x16x32_f16 v[70:73], v[30:33], v[74:77], v[70:73]
	v_mfma_f32_16x16x32_f16 v[30:33], v[30:33], v[18:21], v[50:53]
	s_waitcnt lgkmcnt(0)
	v_mfma_f32_16x16x32_f16 v[50:53], v[58:61], v[66:69], v[10:13]
	v_mfma_f32_16x16x32_f16 v[66:69], v[58:61], v[74:77], v[2:5]
	s_nop 2
	v_bitop3_b32 v2, v1, v84, 20 bitop3:0x36
	v_lshl_or_b32 v100, v2, 4, v87
	ds_read_b128 v[2:5], v100
	ds_read_b128 v[10:13], v100 offset:8192
	s_waitcnt vmcnt(1) lgkmcnt(1)
	v_mfma_f32_16x16x32_f16 v[74:77], v[2:5], v[42:45], v[34:37]
	s_nop 2
	v_add_co_u32_e32 v34, vcc, 0x2000, v82
	v_mfma_f32_16x16x32_f16 v[46:49], v[2:5], v[62:65], v[46:49]
	s_nop 0
	v_addc_co_u32_e32 v35, vcc, 0, v83, vcc
	s_waitcnt vmcnt(0)
	v_mfma_f32_16x16x32_f16 v[88:91], v[2:5], v[78:81], v[22:25]
	ds_read_b128 v[2:5], v100 offset:16384
	ds_read_b128 v[100:103], v100 offset:24576
	s_nop 0
	v_add_co_u32_e32 v22, vcc, 0x4000, v82
	v_mfma_f32_16x16x32_f16 v[58:61], v[58:61], v[18:21], v[6:9]
	s_nop 0
	v_addc_co_u32_e32 v23, vcc, 0, v83, vcc
	v_add_co_u32_e32 v24, vcc, 0x6000, v82
	global_load_dwordx4 v[6:9], v[34:35], off
	s_waitcnt lgkmcnt(2)
	v_mfma_f32_16x16x32_f16 v[96:99], v[10:13], v[78:81], v[14:17]
	v_addc_co_u32_e32 v25, vcc, 0, v83, vcc
	v_lshlrev_b32_e32 v83, 4, v86
	s_nop 0
	global_load_dwordx4 v[14:17], v[22:23], off
	v_mfma_f32_16x16x32_f16 v[92:95], v[10:13], v[42:45], v[26:29]
	v_mfma_f32_16x16x32_f16 v[36:39], v[10:13], v[62:65], v[38:41]
	s_waitcnt lgkmcnt(1)
	v_mfma_f32_16x16x32_f16 v[54:57], v[2:5], v[42:45], v[54:57]
	v_mfma_f32_16x16x32_f16 v[70:73], v[2:5], v[62:65], v[70:73]
	v_mfma_f32_16x16x32_f16 v[104:107], v[2:5], v[78:81], v[30:33]
	global_load_dwordx4 v[18:21], v[24:25], off
	global_load_dwordx4 v[2:5], v[34:35], off offset:1024
	global_load_dwordx4 v[10:13], v[22:23], off offset:1024
	v_bitop3_b32 v22, v1, v84, 24 bitop3:0x36
	v_lshl_or_b32 v82, v22, 4, v87
	global_load_dwordx4 v[22:25], v[24:25], off offset:1024
	v_or_b32_e32 v34, v83, v84
	v_ashrrev_i32_e32 v35, 31, v34
	s_waitcnt lgkmcnt(0)
	v_mfma_f32_16x16x32_f16 v[26:29], v[100:103], v[42:45], v[50:53]
	v_lshl_add_u64 v[44:45], v[34:35], 2, s[28:29]
	global_load_dword v35, v[44:45], off
	ds_read_b128 v[40:43], v82
	ds_read_b128 v[50:53], v82 offset:8192
	v_bitop3_b32 v44, v1, v84, 28 bitop3:0x36
	v_mfma_f32_16x16x32_f16 v[30:33], v[100:103], v[62:65], v[66:69]
	v_lshl_or_b32 v108, v44, 4, v87
	s_waitcnt vmcnt(6) lgkmcnt(1)
	v_mfma_f32_16x16x32_f16 v[62:65], v[40:43], v[6:9], v[74:77]
	s_waitcnt vmcnt(5)
	v_mfma_f32_16x16x32_f16 v[44:47], v[40:43], v[14:17], v[46:49]
	s_waitcnt vmcnt(4)
	v_mfma_f32_16x16x32_f16 v[40:43], v[40:43], v[18:21], v[88:91]
	v_mfma_f32_16x16x32_f16 v[58:61], v[100:103], v[78:81], v[58:61]
	ds_read_b128 v[66:69], v108
	ds_read_b128 v[74:77], v82 offset:16384
	ds_read_b128 v[78:81], v82 offset:24576
	v_lshlrev_b32_e32 v82, 5, v1
	ds_read_b128 v[86:89], v108 offset:8192
	ds_read_b128 v[100:103], v108 offset:16384
	ds_read_b128 v[108:111], v108 offset:24576
	ds_read_b128 v[112:115], v82 offset:39936
	ds_read_b128 v[116:119], v82 offset:39952
	s_waitcnt vmcnt(1) lgkmcnt(7)
	v_mfma_f32_16x16x32_f16 v[40:43], v[66:69], v[22:25], v[40:43]
	v_lshlrev_b32_e32 v1, 11, v1
	v_mfma_f32_16x16x32_f16 v[44:47], v[66:69], v[10:13], v[44:47]
	v_mfma_f32_16x16x32_f16 v[62:65], v[66:69], v[2:5], v[62:65]
	s_waitcnt lgkmcnt(1)
	s_nop 3
	v_mul_f32_e32 v40, v113, v40
	s_nop 0
	v_fmac_f32_e32 v40, v112, v44
	s_waitcnt vmcnt(0)
	v_add_f32_e32 v40, v35, v40
	v_mfma_f32_16x16x32_f16 v[66:69], v[50:53], v[6:9], v[92:95]
	v_mfma_f32_16x16x32_f16 v[36:39], v[50:53], v[14:17], v[36:39]
	v_add_f32_e32 v90, v62, v40
	v_mul_f32_e32 v40, v115, v41
	v_fmac_f32_e32 v40, v114, v45
	v_add_f32_e32 v40, v35, v40
	v_add_f32_e32 v91, v63, v40
	s_waitcnt lgkmcnt(0)
	v_mul_f32_e32 v40, v117, v42
	v_fmac_f32_e32 v40, v116, v46
	v_add_f32_e32 v40, v35, v40
	v_mfma_f32_16x16x32_f16 v[48:51], v[50:53], v[18:21], v[96:99]
	v_add_f32_e32 v92, v64, v40
	v_mul_f32_e32 v40, v119, v43
	v_fmac_f32_e32 v40, v118, v47
	v_add_f32_e32 v40, v35, v40
	v_add_f32_e32 v93, v65, v40
	ds_read_b128 v[40:43], v82 offset:40064
	ds_read_b128 v[44:47], v82 offset:40080
	v_mfma_f32_16x16x32_f16 v[48:51], v[86:89], v[22:25], v[48:51]
	v_mfma_f32_16x16x32_f16 v[36:39], v[86:89], v[10:13], v[36:39]
	v_mfma_f32_16x16x32_f16 v[62:65], v[86:89], v[2:5], v[66:69]
	s_waitcnt lgkmcnt(1)
	s_nop 4
	v_mul_f32_e32 v41, v41, v48
	v_fmac_f32_e32 v41, v40, v36
	v_add_f32_e32 v36, v35, v41
	v_mfma_f32_16x16x32_f16 v[66:69], v[74:77], v[18:21], v[104:107]
	v_mfma_f32_16x16x32_f16 v[18:21], v[78:81], v[18:21], v[58:61]
	v_add_f32_e32 v62, v62, v36
	v_mul_f32_e32 v36, v43, v49
	v_fmac_f32_e32 v36, v42, v37
	v_add_f32_e32 v36, v35, v36
	v_mfma_f32_16x16x32_f16 v[40:43], v[74:77], v[6:9], v[54:57]
	s_nop 2
	v_add_f32_e32 v56, v63, v36
	s_waitcnt lgkmcnt(0)
	v_mul_f32_e32 v36, v45, v50
	v_fmac_f32_e32 v36, v44, v38
	v_mfma_f32_16x16x32_f16 v[52:55], v[74:77], v[14:17], v[70:73]
	v_add_f32_e32 v36, v35, v36
	v_add_f32_e32 v57, v64, v36
	v_mul_f32_e32 v36, v47, v51
	v_fmac_f32_e32 v36, v46, v39
	v_add_f32_e32 v44, v35, v36
	v_mfma_f32_16x16x32_f16 v[36:39], v[100:103], v[10:13], v[52:55]
	v_add_f32_e32 v63, v65, v44
	ds_read_b128 v[44:47], v82 offset:40192
	ds_read_b128 v[48:51], v82 offset:40208
	v_mfma_f32_16x16x32_f16 v[52:55], v[100:103], v[22:25], v[66:69]
	v_mfma_f32_16x16x32_f16 v[40:43], v[100:103], v[2:5], v[40:43]
	v_mfma_f32_16x16x32_f16 v[6:9], v[78:81], v[6:9], v[26:29]
	s_waitcnt lgkmcnt(1)
	s_nop 4
	v_mul_f32_e32 v45, v45, v52
	v_fmac_f32_e32 v45, v44, v36
	v_add_f32_e32 v36, v35, v45
	v_add_f32_e32 v36, v40, v36
	v_mul_f32_e32 v40, v47, v53
	v_fmac_f32_e32 v40, v46, v37
	v_add_f32_e32 v26, v35, v40
	v_add_f32_e32 v37, v41, v26
	s_waitcnt lgkmcnt(0)
	v_mul_f32_e32 v26, v49, v54
	v_fmac_f32_e32 v26, v48, v38
	v_mfma_f32_16x16x32_f16 v[14:17], v[78:81], v[14:17], v[30:33]
	v_add_f32_e32 v26, v35, v26
	s_nop 1
	v_add_f32_e32 v30, v42, v26
	v_mul_f32_e32 v26, v51, v55
	v_fmac_f32_e32 v26, v50, v39
	v_add_f32_e32 v26, v35, v26
	v_mfma_f32_16x16x32_f16 v[10:13], v[108:111], v[10:13], v[14:17]
	v_add_f32_e32 v31, v43, v26
	s_nop 1
	ds_read_b128 v[14:17], v82 offset:40320
	ds_read_b128 v[26:29], v82 offset:40336
	s_waitcnt lgkmcnt(0)
	v_mfma_f32_16x16x32_f16 v[18:21], v[108:111], v[22:25], v[18:21]
	s_barrier
	v_mfma_f32_16x16x32_f16 v[2:5], v[108:111], v[2:5], v[6:9]
	s_nop 2
	v_max_f32_e32 v7, 0, v90
	s_nop 1
	v_mul_f32_e32 v6, v17, v19
	v_fmac_f32_e32 v6, v16, v11
	v_add_f32_e32 v6, v35, v6
	v_add_f32_e32 v3, v3, v6
	v_mul_f32_e32 v6, v27, v20
	v_fmac_f32_e32 v6, v26, v12
	v_cvt_f16_f32_e32 v7, v7
	v_add_f32_e32 v6, v35, v6
	v_bitop3_b32 v8, v82, v34, -8 bitop3:0x78
	v_add_f32_e32 v4, v4, v6
	v_mul_f32_e32 v6, v29, v21
	v_lshl_add_u32 v8, v8, 1, v1
	v_lshlrev_b32_e32 v9, 1, v85
	v_mul_f32_e32 v15, v15, v18
	v_fmac_f32_e32 v6, v28, v13
	v_or_b32_e32 v8, v8, v9
	v_fmac_f32_e32 v15, v14, v10
	v_add_f32_e32 v6, v35, v6
	ds_write_b16 v8, v7
	v_max_f32_e32 v7, 0, v91
	v_add_f32_e32 v10, v35, v15
	v_add_f32_e32 v5, v5, v6
	v_bitop3_b32 v6, v83, -8, v84 bitop3:0xc8
	v_cvt_f16_f32_e32 v7, v7
	v_add_f32_e32 v2, v2, v10
	v_bitop3_b32 v10, v82, v6, 8 bitop3:0x36
	v_lshl_add_u32 v10, v10, 1, v1
	v_or_b32_e32 v10, v10, v9
	ds_write_b16 v10, v7 offset:512
	v_max_f32_e32 v7, 0, v92
	v_cvt_f16_f32_e32 v7, v7
	v_bitop3_b32 v11, v82, v6, 16 bitop3:0x36
	v_lshl_add_u32 v11, v11, 1, v1
	v_or_b32_e32 v11, v11, v9
	ds_write_b16 v11, v7 offset:1024
	v_max_f32_e32 v7, 0, v93
	v_cvt_f16_f32_e32 v7, v7
	v_bitop3_b32 v6, v82, v6, 24 bitop3:0x36
	v_lshl_add_u32 v1, v6, 1, v1
	v_or_b32_e32 v1, v1, v9
	v_max_f32_e32 v6, 0, v62
	ds_write_b16 v1, v7 offset:1536
	v_cvt_f16_f32_e32 v6, v6
	v_max_f32_e32 v7, 0, v56
	v_cvt_f16_f32_e32 v7, v7
	v_max_f32_e32 v9, 0, v57
	v_cvt_f16_f32_e32 v9, v9
	v_max_f32_e32 v12, 0, v63
	v_cvt_f16_f32_e32 v12, v12
	ds_write_b16 v8, v6 offset:8192
	ds_write_b16 v10, v7 offset:8704
	ds_write_b16 v11, v9 offset:9216
	ds_write_b16 v1, v12 offset:9728
	v_max_f32_e32 v6, 0, v36
	v_max_f32_e32 v2, 0, v2
	v_cvt_f16_f32_e32 v6, v6
	v_max_f32_e32 v7, 0, v37
	v_cvt_f16_f32_e32 v2, v2
	v_max_f32_e32 v3, 0, v3
	v_cvt_f16_f32_e32 v7, v7
	v_max_f32_e32 v9, 0, v30
	v_cvt_f16_f32_e32 v3, v3
	v_max_f32_e32 v4, 0, v4
	v_cvt_f16_f32_e32 v9, v9
	v_max_f32_e32 v12, 0, v31
	v_cvt_f16_f32_e32 v4, v4
	v_max_f32_e32 v5, 0, v5
	v_cvt_f16_f32_e32 v12, v12
	v_cvt_f16_f32_e32 v5, v5
	ds_write_b16 v8, v6 offset:16384
	ds_write_b16 v10, v7 offset:16896
	ds_write_b16 v11, v9 offset:17408
	ds_write_b16 v1, v12 offset:17920
	ds_write_b16 v8, v2 offset:24576
	ds_write_b16 v10, v3 offset:25088
	ds_write_b16 v11, v4 offset:25600
	ds_write_b16 v1, v5 offset:26112
	s_waitcnt lgkmcnt(0)
	s_barrier
	s_nop 0
	v_ashrrev_i32_e32 v36, 3, v0
	v_lshlrev_b32_e32 v1, 2, v36
	ds_read_b32 v34, v1 offset:40448
	v_and_b32_e32 v1, 7, v0
	v_lshlrev_b32_e32 v37, 3, v1
	s_cbranch_scc1 .LBB2_62
	s_waitcnt lgkmcnt(0)
	v_cmp_lt_i32_e32 vcc, -1, v34
	s_and_saveexec_b64 s[0:1], vcc
	s_cbranch_execz .LBB2_37
	v_lshrrev_b32_e32 v2, 3, v0
	v_mov_b32_e32 v35, 0
	v_bitop3_b32 v2, v2, v1, 15 bitop3:0x6c
	v_lshlrev_b64 v[6:7], 7, v[34:35]
	v_lshlrev_b32_e32 v2, 4, v2
	v_lshl_or_b32 v2, v36, 9, v2
	v_lshl_add_u64 v[6:7], s[26:27], 0, v[6:7]
	v_lshlrev_b32_e32 v8, 1, v37
	v_mov_b32_e32 v9, v35
	ds_read_b128 v[2:5], v2
	v_lshl_add_u64 v[6:7], v[6:7], 0, v[8:9]
	s_waitcnt lgkmcnt(0)
	global_store_dwordx4 v[6:7], v[2:5], off sc1
	s_nop 1

_Z5k_aggILi1EEvPKDF16_S1_S1_PK15HIP_vector_typeIiLj4EEPKiS7_PKfS1_S9_PfPDF16_S1_S9_SB_SB_:
	s_lshr_b32 s3, s2, 3
	s_bitcmp1_b32 s3, 3
	s_cbranch_scc0 .Lnosleep_a1_0
	s_sleep 127
	s_sleep 23
.Lnosleep_a1_0:
	s_load_dwordx2 s[6:7], s[0:1], 0x30
	s_load_dwordx2 s[4:5], s[0:1], 0x18
	s_load_dwordx4 s[20:23], s[0:1], 0x20
	s_load_dwordx2 s[24:25], s[0:1], 0x10
	s_load_dwordx4 s[16:19], s[0:1], 0x0
	s_and_b32 s26, s2, 7
	s_lshr_b32 s27, s2, 3
	s_mul_i32 s28, s26, 0x61
	s_min_u32 s26, s26, 6
	s_add_i32 s30, s26, s27
	s_add_i32 s30, s30, s28
	v_lshrrev_b32_e32 v100, 3, v0
	v_and_b32_e32 v101, 7, v0
	v_lshl_or_b32 v102, s30, 6, v100
	v_mov_b32_e32 v103, 0
	v_and_b32_e32 v1, 63, v0
	v_lshlrev_b32_e32 v2, 2, v1
	v_or_b32_e32 v16, 0x300, v1
	v_lshlrev_b32_e32 v104, 5, v102
	v_lshl_or_b32 v104, v101, 2, v104
	s_waitcnt lgkmcnt(0)
	v_lshl_add_u64 v[106:107], v[102:103], 4, s[4:5]
	global_load_dwordx3 v[42:44], v[106:107], off
	global_load_dwordx3 v[46:48], v[106:107], off offset:512
	global_load_dword v45, v104, s[22:23]
	global_load_dword v49, v104, s[22:23] offset:1024
	global_load_dword v4, v2, s[6:7]
	global_load_dword v5, v2, s[6:7] offset:256
	global_load_dword v6, v2, s[6:7] offset:512
	global_load_dword v7, v2, s[6:7] offset:768
	global_load_dword v8, v2, s[6:7] offset:1024
	global_load_dword v9, v2, s[6:7] offset:1280
	global_load_dword v10, v2, s[6:7] offset:1536
	global_load_dword v11, v2, s[6:7] offset:1792
	global_load_dword v12, v2, s[6:7] offset:2048
	global_load_dword v13, v2, s[6:7] offset:2304
	global_load_dword v14, v2, s[6:7] offset:2560
	global_load_dword v15, v2, s[6:7] offset:2816
	s_movk_i32 s3, 0x30e
	v_mov_b32_e32 v3, 0
	v_cmp_gt_u32_e32 vcc, s3, v16
	s_waitcnt vmcnt(11)
	v_add_f32_e32 v1, 0, v4
	s_waitcnt vmcnt(10)
	v_add_f32_e32 v1, v1, v5
	s_waitcnt vmcnt(9)
	v_add_f32_e32 v1, v1, v6
	s_waitcnt vmcnt(8)
	v_add_f32_e32 v1, v1, v7
	s_waitcnt vmcnt(7)
	v_add_f32_e32 v1, v1, v8
	s_waitcnt vmcnt(6)
	v_add_f32_e32 v1, v1, v9
	s_waitcnt vmcnt(5)
	v_add_f32_e32 v1, v1, v10
	s_waitcnt vmcnt(4)
	v_add_f32_e32 v1, v1, v11
	s_waitcnt vmcnt(3)
	v_add_f32_e32 v1, v1, v12
	s_waitcnt vmcnt(2)
	v_add_f32_e32 v1, v1, v13
	s_waitcnt vmcnt(1)
	v_add_f32_e32 v1, v1, v14
	s_waitcnt vmcnt(0)
	v_add_f32_e32 v1, v1, v15
	s_and_saveexec_b64 s[8:9], vcc
	s_cbranch_execz .LBB3_2
	v_lshl_add_u64 v[4:5], s[6:7], 0, v[2:3]
	global_load_dword v2, v[4:5], off offset:3072
	s_waitcnt vmcnt(0)
	v_add_f32_e32 v1, v1, v2

.Lpl_last_a1:
	s_waitcnt vmcnt(6)
	s_mov_b64 exec, s[44:45]
	v_pk_minimum3_f16 v52, v52, v10, v14
	v_pk_maximum3_f16 v100, v100, v10, v14
	v_pk_minimum3_f16 v99, v99, v11, v15
	v_pk_maximum3_f16 v101, v101, v11, v15
	v_pk_minimum3_f16 v98, v98, v12, v16
	v_pk_maximum3_f16 v105, v105, v12, v16
	v_pk_minimum3_f16 v103, v103, v13, v17
	v_pk_maximum3_f16 v104, v104, v13, v17
	v_pk_mul_f16 v110, v10, v10
	v_mov_b32_e32 v106, v10
	v_pk_mul_f16 v111, v11, v11
	v_mov_b32_e32 v107, v11
	v_pk_mul_f16 v112, v12, v12
	v_mov_b32_e32 v108, v12
	v_pk_mul_f16 v113, v13, v13
	v_mov_b32_e32 v109, v13
	s_mov_b64 exec, s[46:47]
	v_pk_add_f16 v106, v106, v14
	v_pk_fma_f16 v110, v14, v14, v110
	v_pk_add_f16 v107, v107, v15
	v_pk_fma_f16 v111, v15, v15, v111
	v_pk_add_f16 v108, v108, v16
	v_pk_fma_f16 v112, v16, v16, v112
	v_pk_add_f16 v109, v109, v17
	v_pk_fma_f16 v113, v17, v17, v113
	s_mov_b64 exec, -1
	s_waitcnt vmcnt(4)
	s_mov_b64 exec, s[48:49]
	v_pk_minimum3_f16 v52, v52, v18, v22
	v_pk_maximum3_f16 v100, v100, v18, v22
	v_pk_minimum3_f16 v99, v99, v19, v23
	v_pk_maximum3_f16 v101, v101, v19, v23
	v_pk_minimum3_f16 v98, v98, v20, v24
	v_pk_maximum3_f16 v105, v105, v20, v24
	v_pk_minimum3_f16 v103, v103, v21, v25
	v_pk_maximum3_f16 v104, v104, v21, v25
	v_pk_add_f16 v106, v106, v18
	v_pk_fma_f16 v110, v18, v18, v110
	v_pk_add_f16 v107, v107, v19
	v_pk_fma_f16 v111, v19, v19, v111
	v_pk_add_f16 v108, v108, v20
	v_pk_fma_f16 v112, v20, v20, v112
	v_pk_add_f16 v109, v109, v21
	v_pk_fma_f16 v113, v21, v21, v113
	s_mov_b64 exec, s[50:51]
	v_pk_add_f16 v106, v106, v22
	v_pk_fma_f16 v110, v22, v22, v110
	v_pk_add_f16 v107, v107, v23
	v_pk_fma_f16 v111, v23, v23, v111
	v_pk_add_f16 v108, v108, v24
	v_pk_fma_f16 v112, v24, v24, v112
	v_pk_add_f16 v109, v109, v25
	v_pk_fma_f16 v113, v25, v25, v113
	s_mov_b64 exec, -1
	s_waitcnt vmcnt(2)
	s_mov_b64 exec, s[52:53]
	v_pk_minimum3_f16 v52, v52, v26, v30
	v_pk_maximum3_f16 v100, v100, v26, v30
	v_pk_minimum3_f16 v99, v99, v27, v31
	v_pk_maximum3_f16 v101, v101, v27, v31
	v_pk_minimum3_f16 v98, v98, v28, v32
	v_pk_maximum3_f16 v105, v105, v28, v32
	v_pk_minimum3_f16 v103, v103, v29, v33
	v_pk_maximum3_f16 v104, v104, v29, v33
	v_pk_add_f16 v106, v106, v26
	v_pk_fma_f16 v110, v26, v26, v110
	v_pk_add_f16 v107, v107, v27
	v_pk_fma_f16 v111, v27, v27, v111
	v_pk_add_f16 v108, v108, v28
	v_pk_fma_f16 v112, v28, v28, v112
	v_pk_add_f16 v109, v109, v29
	v_pk_fma_f16 v113, v29, v29, v113
	s_mov_b64 exec, s[54:55]
	v_pk_add_f16 v106, v106, v30
	v_pk_fma_f16 v110, v30, v30, v110
	v_pk_add_f16 v107, v107, v31
	v_pk_fma_f16 v111, v31, v31, v111
	v_pk_add_f16 v108, v108, v32
	v_pk_fma_f16 v112, v32, v32, v112
	v_pk_add_f16 v109, v109, v33
	v_pk_fma_f16 v113, v33, v33, v113
	s_mov_b64 exec, -1
	s_waitcnt vmcnt(0)
	s_mov_b64 exec, s[56:57]
	v_pk_minimum3_f16 v52, v52, v34, v38
	v_pk_maximum3_f16 v100, v100, v34, v38
	v_pk_minimum3_f16 v99, v99, v35, v39
	v_pk_maximum3_f16 v101, v101, v35, v39
	v_pk_minimum3_f16 v98, v98, v36, v40
	v_pk_maximum3_f16 v105, v105, v36, v40
	v_pk_minimum3_f16 v103, v103, v37, v41
	v_pk_maximum3_f16 v104, v104, v37, v41
	v_pk_add_f16 v106, v106, v34
	v_pk_fma_f16 v110, v34, v34, v110
	v_pk_add_f16 v107, v107, v35
	v_pk_fma_f16 v111, v35, v35, v111
	v_pk_add_f16 v108, v108, v36
	v_pk_fma_f16 v112, v36, v36, v112
	v_pk_add_f16 v109, v109, v37
	v_pk_fma_f16 v113, v37, v37, v113
	s_mov_b64 exec, s[58:59]
	v_pk_add_f16 v106, v106, v38
	v_pk_fma_f16 v110, v38, v38, v110
	v_pk_add_f16 v107, v107, v39
	v_pk_fma_f16 v111, v39, v39, v111
	v_pk_add_f16 v108, v108, v40
	v_pk_fma_f16 v112, v40, v40, v112
	v_pk_add_f16 v109, v109, v41
	v_pk_fma_f16 v113, v41, v41, v113
	s_mov_b64 exec, -1
	s_mov_b64 exec, s[44:45]
	v_cvt_f32_f16_e32 v114, v106
	v_cvt_f32_f16_sdwa v115, v106 dst_sel:DWORD dst_unused:UNUSED_PAD src0_sel:WORD_1
	v_cvt_f32_f16_e32 v118, v110
	v_cvt_f32_f16_sdwa v119, v110 dst_sel:DWORD dst_unused:UNUSED_PAD src0_sel:WORD_1
	v_pk_add_f32 v[72:73], v[72:73], v[114:115]
	v_cvt_f32_f16_e32 v114, v107
	v_cvt_f32_f16_sdwa v115, v107 dst_sel:DWORD dst_unused:UNUSED_PAD src0_sel:WORD_1
	v_pk_add_f32 v[76:77], v[76:77], v[118:119]
	v_cvt_f32_f16_e32 v118, v111
	v_cvt_f32_f16_sdwa v119, v111 dst_sel:DWORD dst_unused:UNUSED_PAD src0_sel:WORD_1
	v_pk_add_f32 v[70:71], v[70:71], v[114:115]
	v_cvt_f32_f16_e32 v114, v108
	v_cvt_f32_f16_sdwa v115, v108 dst_sel:DWORD dst_unused:UNUSED_PAD src0_sel:WORD_1
	v_pk_add_f32 v[74:75], v[74:75], v[118:119]
	v_cvt_f32_f16_e32 v118, v112
	v_cvt_f32_f16_sdwa v119, v112 dst_sel:DWORD dst_unused:UNUSED_PAD src0_sel:WORD_1
	v_pk_add_f32 v[64:65], v[64:65], v[114:115]
	v_cvt_f32_f16_e32 v114, v109
	v_cvt_f32_f16_sdwa v115, v109 dst_sel:DWORD dst_unused:UNUSED_PAD src0_sel:WORD_1
	v_pk_add_f32 v[68:69], v[68:69], v[118:119]
	v_cvt_f32_f16_e32 v118, v113
	v_cvt_f32_f16_sdwa v119, v113 dst_sel:DWORD dst_unused:UNUSED_PAD src0_sel:WORD_1
	v_pk_add_f32 v[62:63], v[62:63], v[114:115]
	s_nop 0
	v_pk_add_f32 v[66:67], v[66:67], v[118:119]
	s_mov_b64 exec, -1
	s_waitcnt vmcnt(0)
	s_cmp_eq_u64 s[4:5], 0
	s_cbranch_scc0 .Lnowp_a1
	v_readfirstlane_b32 s60, v0
	v_and_b32_e32 v79, 63, v0
	s_nop 3
	s_lshr_b32 s60, s60, 6
	s_mul_i32 s60, s60, 0x6800
	s_add_u32 s62, s12, s60
	s_addc_u32 s63, s13, 0
	v_lshlrev_b32_e32 v79, 4, v79
	global_load_dwordx4 v[88:91], v79, s[62:63]
	global_load_dwordx4 v[106:109], v79, s[62:63] offset:1024
	global_load_dwordx4 v[110:113], v79, s[62:63] offset:2048
	global_load_dwordx4 v[114:117], v79, s[62:63] offset:3072

.LBB3_30:
	s_or_b64 exec, exec, s[2:3]
	v_ashrrev_i32_e32 v85, 6, v0
	v_mul_lo_u32 v4, v85, 26
	v_ashrrev_i32_e32 v5, 31, v4
	v_lshlrev_b64 v[4:5], 10, v[4:5]
	v_lshl_add_u64 v[4:5], s[12:13], 0, v[4:5]
	v_lshlrev_b32_e32 v2, 4, v6
	v_lshl_add_u64 v[82:83], v[4:5], 0, v[2:3]
	s_movk_i32 s2, 0x2000
	v_add_co_u32_e32 v2, vcc, s2, v82
	s_movk_i32 s2, 0x4000
	s_nop 0
	v_addc_co_u32_e32 v3, vcc, 0, v83, vcc
	v_add_co_u32_e32 v4, vcc, s2, v82
	s_movk_i32 s2, 0x1000
	s_nop 0
	v_addc_co_u32_e32 v5, vcc, 0, v83, vcc
	global_load_dwordx4 v[42:45], v[2:3], off offset:2048
	global_load_dwordx4 v[18:21], v[2:3], off offset:3072
	global_load_dwordx4 v[46:49], v[4:5], off offset:2048
	global_load_dwordx4 v[26:29], v[4:5], off offset:3072
	v_add_co_u32_e32 v2, vcc, s2, v82
	s_movk_i32 s2, 0x3000
	s_nop 0
	v_addc_co_u32_e32 v3, vcc, 0, v83, vcc
	v_add_co_u32_e32 v4, vcc, s2, v82
	s_movk_i32 s2, 0x5000
	s_nop 0
	v_addc_co_u32_e32 v5, vcc, 0, v83, vcc
	v_add_co_u32_e32 v66, vcc, s2, v82
	v_mov_b32_e32 v80, 0x8000
	s_nop 0
	v_addc_co_u32_e32 v67, vcc, 0, v83, vcc
	global_load_dwordx4 v[22:25], v[2:3], off
	global_load_dwordx4 v[6:9], v[2:3], off offset:1024
	global_load_dwordx4 v[30:33], v[4:5], off
	global_load_dwordx4 v[10:13], v[4:5], off offset:1024
	global_load_dwordx4 v[34:37], v[66:67], off
	s_nop 0
	global_load_dwordx4 v[2:5], v[66:67], off offset:1024
	v_bitop3_b32 v66, v0, v1, 7 bitop3:0x6c
	v_lshl_or_b32 v78, v84, 7, v80
	v_lshl_or_b32 v74, v66, 4, v78
	s_waitcnt vmcnt(12)
	v_mov_b32_e32 v62, v88
	v_mov_b32_e32 v63, v89
	v_mov_b32_e32 v64, v90
	v_mov_b32_e32 v65, v91
	v_mov_b32_e32 v58, v106
	v_mov_b32_e32 v59, v107
	v_mov_b32_e32 v60, v108
	v_mov_b32_e32 v61, v109
	v_mov_b32_e32 v38, v110
	v_mov_b32_e32 v39, v111
	v_mov_b32_e32 v40, v112
	v_mov_b32_e32 v41, v113
	v_mov_b32_e32 v14, v114
	v_mov_b32_e32 v15, v115
	v_mov_b32_e32 v16, v116
	v_mov_b32_e32 v17, v117
	s_waitcnt lgkmcnt(0)
	s_barrier
	ds_read_b128 v[66:69], v74
	ds_read_b128 v[70:73], v74 offset:2048
	ds_read_b128 v[74:77], v74 offset:4096
	v_or_b32_e32 v81, 48, v84
	v_min_u32_e32 v81, 55, v81
	v_and_b32_e32 v79, 7, v0
	v_and_b32_e32 v86, 7, v81
	v_lshl_or_b32 v87, v81, 7, v80
	s_waitcnt vmcnt(10) lgkmcnt(2)
	v_mfma_f32_16x16x32_f16 v[66:69], v[66:69], v[62:65], 0
	s_waitcnt lgkmcnt(1)
	v_mfma_f32_16x16x32_f16 v[70:73], v[70:73], v[62:65], 0
	s_waitcnt lgkmcnt(0)
	v_mfma_f32_16x16x32_f16 v[74:77], v[74:77], v[62:65], 0
	s_and_saveexec_b64 s[2:3], s[0:1]
	v_xor_b32_e32 v54, v86, v1
	v_lshl_add_u32 v54, v54, 4, v87
	ds_read_b128 v[54:57], v54
	s_or_b64 exec, exec, s[2:3]
	v_bitop3_b32 v79, v79, v1, 4 bitop3:0x1e
	v_lshl_add_u32 v92, v79, 4, v78
	ds_read_b128 v[88:91], v92
	s_waitcnt lgkmcnt(1)
	v_mfma_f32_16x16x32_f16 v[78:81], v[54:57], v[62:65], 0
	ds_read_b128 v[54:57], v92 offset:2048
	s_waitcnt vmcnt(12) lgkmcnt(0)
	v_mfma_f32_16x16x32_f16 v[62:65], v[54:57], v[58:61], v[70:73]
	ds_read_b128 v[54:57], v92 offset:4096
	s_nop 1
	v_or_b32_e32 v70, 4, v1
	v_mfma_f32_16x16x32_f16 v[66:69], v[88:91], v[58:61], v[66:69]
	s_waitcnt lgkmcnt(0)
	v_mfma_f32_16x16x32_f16 v[54:57], v[54:57], v[58:61], v[74:77]
	s_and_saveexec_b64 s[2:3], s[0:1]
	v_xor_b32_e32 v50, v86, v70
	v_lshl_add_u32 v50, v50, 4, v87
	ds_read_b128 v[50:53], v50
	s_or_b64 exec, exec, s[2:3]
	s_waitcnt lgkmcnt(0)
	v_mfma_f32_16x16x32_f16 v[50:53], v[50:53], v[58:61], v[78:81]
	v_lshlrev_b32_e32 v104, 9, v84
	v_xor_b32_e32 v58, v1, v84
	v_lshl_or_b32 v71, v58, 4, v104
	ds_read_b128 v[58:61], v71
	ds_read_b128 v[72:75], v71 offset:8192
	ds_read_b128 v[90:93], v71 offset:16384
	ds_read_b128 v[94:97], v71 offset:24576
	s_waitcnt vmcnt(11) lgkmcnt(3)
	v_mfma_f32_16x16x32_f16 v[66:69], v[58:61], v[38:41], v[66:69]
	s_cmpk_lt_u32 s30, 0x30c
	s_waitcnt lgkmcnt(2)
	v_mfma_f32_16x16x32_f16 v[62:65], v[72:75], v[38:41], v[62:65]
	s_waitcnt lgkmcnt(1)
	v_mfma_f32_16x16x32_f16 v[54:57], v[90:93], v[38:41], v[54:57]
	s_waitcnt lgkmcnt(0)
	v_mfma_f32_16x16x32_f16 v[38:41], v[94:97], v[38:41], v[50:53]
	s_nop 2
	v_xor_b32_e32 v50, v70, v84
	v_lshl_or_b32 v80, v50, 4, v104
	s_waitcnt vmcnt(9)
	v_mfma_f32_16x16x32_f16 v[76:79], v[58:61], v[42:45], 0
	s_waitcnt vmcnt(7)
	v_mfma_f32_16x16x32_f16 v[58:61], v[58:61], v[46:49], 0
	v_mfma_f32_16x16x32_f16 v[86:89], v[72:75], v[42:45], 0
	v_mfma_f32_16x16x32_f16 v[72:75], v[72:75], v[46:49], 0
	v_mfma_f32_16x16x32_f16 v[98:101], v[90:93], v[42:45], 0
	v_mfma_f32_16x16x32_f16 v[90:93], v[90:93], v[46:49], 0
	v_mfma_f32_16x16x32_f16 v[42:45], v[94:97], v[42:45], 0
	v_mfma_f32_16x16x32_f16 v[46:49], v[94:97], v[46:49], 0
	ds_read_b128 v[50:53], v80
	ds_read_b128 v[94:97], v80 offset:8192
	s_waitcnt lgkmcnt(1)
	v_mfma_f32_16x16x32_f16 v[66:69], v[50:53], v[14:17], v[66:69]
	v_mfma_f32_16x16x32_f16 v[76:79], v[50:53], v[18:21], v[76:79]
	s_waitcnt vmcnt(6)
	v_mfma_f32_16x16x32_f16 v[50:53], v[50:53], v[26:29], v[58:61]
	s_waitcnt lgkmcnt(0)
	v_mfma_f32_16x16x32_f16 v[58:61], v[94:97], v[14:17], v[62:65]
	v_mfma_f32_16x16x32_f16 v[62:65], v[94:97], v[18:21], v[86:89]
	v_mfma_f32_16x16x32_f16 v[70:73], v[94:97], v[26:29], v[72:75]
	s_nop 1
	ds_read_b128 v[86:89], v80 offset:16384
	ds_read_b128 v[94:97], v80 offset:24576
	s_waitcnt lgkmcnt(1)
	v_mfma_f32_16x16x32_f16 v[54:57], v[86:89], v[14:17], v[54:57]
	s_waitcnt lgkmcnt(0)
	v_mfma_f32_16x16x32_f16 v[14:17], v[94:97], v[14:17], v[38:41]
	s_nop 2
	v_bitop3_b32 v38, v1, v84, 8 bitop3:0x36
	v_lshl_or_b32 v74, v38, 4, v104
	v_mfma_f32_16x16x32_f16 v[98:101], v[86:89], v[18:21], v[98:101]
	v_mfma_f32_16x16x32_f16 v[18:21], v[94:97], v[18:21], v[42:45]
	ds_read_b128 v[38:41], v74
	s_nop 1
	ds_read_b128 v[42:45], v74 offset:8192
	v_mfma_f32_16x16x32_f16 v[86:89], v[86:89], v[26:29], v[90:93]
	v_mfma_f32_16x16x32_f16 v[26:29], v[94:97], v[26:29], v[46:49]
	s_waitcnt vmcnt(5) lgkmcnt(1)
	v_mfma_f32_16x16x32_f16 v[46:49], v[38:41], v[22:25], v[66:69]
	s_waitcnt vmcnt(3)
	v_mfma_f32_16x16x32_f16 v[66:69], v[38:41], v[30:33], v[76:79]
	s_waitcnt vmcnt(1)
	v_mfma_f32_16x16x32_f16 v[38:41], v[38:41], v[34:37], v[50:53]
	s_nop 0
	v_add_co_u32_e32 v78, vcc, 0x1000, v82
	s_waitcnt lgkmcnt(0)
	v_mfma_f32_16x16x32_f16 v[50:53], v[42:45], v[22:25], v[58:61]
	v_addc_co_u32_e32 v79, vcc, 0, v83, vcc
	v_add_co_u32_e32 v80, vcc, 0x3000, v82
	v_mfma_f32_16x16x32_f16 v[58:61], v[42:45], v[30:33], v[62:65]
	s_nop 0
	v_addc_co_u32_e32 v81, vcc, 0, v83, vcc
	v_mfma_f32_16x16x32_f16 v[42:45], v[42:45], v[34:37], v[70:73]
	ds_read_b128 v[62:65], v74 offset:16384
	s_nop 1
	ds_read_b128 v[70:73], v74 offset:24576
	s_waitcnt lgkmcnt(1)
	v_mfma_f32_16x16x32_f16 v[54:57], v[62:65], v[22:25], v[54:57]
	s_waitcnt lgkmcnt(0)
	v_mfma_f32_16x16x32_f16 v[14:17], v[70:73], v[22:25], v[14:17]
	v_mfma_f32_16x16x32_f16 v[22:25], v[70:73], v[34:37], v[26:29]
	s_nop 2
	v_bitop3_b32 v26, v1, v84, 12 bitop3:0x36
	v_mfma_f32_16x16x32_f16 v[18:21], v[70:73], v[30:33], v[18:21]
	v_lshl_or_b32 v70, v26, 4, v104
	v_mfma_f32_16x16x32_f16 v[74:77], v[62:65], v[30:33], v[98:101]
	ds_read_b128 v[26:29], v70
	ds_read_b128 v[30:33], v70 offset:8192
	v_mfma_f32_16x16x32_f16 v[62:65], v[62:65], v[34:37], v[86:89]
	s_waitcnt lgkmcnt(1)
	v_mfma_f32_16x16x32_f16 v[34:37], v[26:29], v[6:9], v[46:49]
	s_nop 0
	v_add_co_u32_e32 v86, vcc, 0x5000, v82
	v_mfma_f32_16x16x32_f16 v[46:49], v[26:29], v[10:13], v[66:69]
	s_nop 0
	v_addc_co_u32_e32 v87, vcc, 0, v83, vcc
	v_add_co_u32_e32 v102, vcc, 0x2000, v82
	s_waitcnt vmcnt(0)
	v_mfma_f32_16x16x32_f16 v[26:29], v[26:29], v[2:5], v[38:41]
	global_load_dwordx4 v[66:69], v[78:79], off offset:2048
	v_addc_co_u32_e32 v103, vcc, 0, v83, vcc
	s_waitcnt lgkmcnt(0)
	v_mfma_f32_16x16x32_f16 v[38:41], v[30:33], v[6:9], v[50:53]
	v_mfma_f32_16x16x32_f16 v[50:53], v[30:33], v[10:13], v[58:61]
	s_nop 2
	ds_read_b128 v[58:61], v70 offset:16384
	v_mfma_f32_16x16x32_f16 v[30:33], v[30:33], v[2:5], v[42:45]
	s_nop 2
	ds_read_b128 v[42:45], v70 offset:24576
	s_waitcnt lgkmcnt(1)
	v_mfma_f32_16x16x32_f16 v[54:57], v[58:61], v[6:9], v[54:57]
	v_mfma_f32_16x16x32_f16 v[70:73], v[58:61], v[10:13], v[74:77]
	s_nop 2
	global_load_dwordx4 v[74:77], v[80:81], off offset:2048
	s_waitcnt lgkmcnt(0)
	v_mfma_f32_16x16x32_f16 v[6:9], v[42:45], v[6:9], v[14:17]
	s_nop 2
	global_load_dwordx4 v[14:17], v[86:87], off offset:2048
	v_mfma_f32_16x16x32_f16 v[58:61], v[58:61], v[2:5], v[62:65]
	v_mfma_f32_16x16x32_f16 v[2:5], v[42:45], v[2:5], v[22:25]
	s_nop 1
	global_load_dwordx4 v[62:65], v[80:81], off offset:3072
	global_load_dwordx4 v[22:25], v[78:79], off offset:3072
	v_mfma_f32_16x16x32_f16 v[10:13], v[42:45], v[10:13], v[18:21]
	global_load_dwordx4 v[78:81], v[86:87], off offset:3072
	s_nop 1
	v_bitop3_b32 v18, v1, v84, 16 bitop3:0x36
	v_lshl_or_b32 v88, v18, 4, v104
	ds_read_b128 v[18:21], v88
	ds_read_b128 v[42:45], v88 offset:8192
	s_waitcnt vmcnt(5) lgkmcnt(1)
	v_mfma_f32_16x16x32_f16 v[34:37], v[18:21], v[66:69], v[34:37]
	s_waitcnt vmcnt(4)
	v_mfma_f32_16x16x32_f16 v[46:49], v[18:21], v[74:77], v[46:49]
	s_waitcnt vmcnt(3)
	v_mfma_f32_16x16x32_f16 v[18:21], v[18:21], v[14:17], v[26:29]
	s_waitcnt lgkmcnt(0)
	v_mfma_f32_16x16x32_f16 v[26:29], v[42:45], v[66:69], v[38:41]
	v_mfma_f32_16x16x32_f16 v[38:41], v[42:45], v[74:77], v[50:53]
	v_mfma_f32_16x16x32_f16 v[30:33], v[42:45], v[14:17], v[30:33]
	ds_read_b128 v[42:45], v88 offset:16384
	s_nop 0
	ds_read_b128 v[50:53], v88 offset:24576
	s_waitcnt lgkmcnt(1)
	v_mfma_f32_16x16x32_f16 v[54:57], v[42:45], v[66:69], v[54:57]
	v_mfma_f32_16x16x32_f16 v[70:73], v[42:45], v[74:77], v[70:73]
	v_mfma_f32_16x16x32_f16 v[42:45], v[42:45], v[14:17], v[58:61]
	s_waitcnt lgkmcnt(0)
	v_mfma_f32_16x16x32_f16 v[58:61], v[50:53], v[66:69], v[6:9]
	s_nop 2
	v_bitop3_b32 v6, v1, v84, 20 bitop3:0x36
	v_mfma_f32_16x16x32_f16 v[66:69], v[50:53], v[74:77], v[10:13]
	s_nop 2
	v_lshl_or_b32 v10, v6, 4, v104
	v_mfma_f32_16x16x32_f16 v[50:53], v[50:53], v[14:17], v[2:5]
	s_nop 2
	ds_read_b128 v[2:5], v10
	ds_read_b128 v[6:9], v10 offset:8192
	ds_read_b128 v[14:17], v10 offset:16384
	ds_read_b128 v[94:97], v10 offset:24576
	s_waitcnt vmcnt(1) lgkmcnt(3)
	v_mfma_f32_16x16x32_f16 v[34:37], v[2:5], v[22:25], v[34:37]
	v_mfma_f32_16x16x32_f16 v[46:49], v[2:5], v[62:65], v[46:49]
	s_waitcnt vmcnt(0)
	v_mfma_f32_16x16x32_f16 v[74:77], v[2:5], v[78:81], v[18:21]
	global_load_dwordx4 v[2:5], v[102:103], off
	s_waitcnt lgkmcnt(2)
	v_mfma_f32_16x16x32_f16 v[86:89], v[6:9], v[22:25], v[26:29]
	s_nop 2
	v_add_co_u32_e32 v26, vcc, 0x4000, v82
	v_mfma_f32_16x16x32_f16 v[38:41], v[6:9], v[62:65], v[38:41]
	s_nop 0
	v_addc_co_u32_e32 v27, vcc, 0, v83, vcc
	v_add_co_u32_e32 v82, vcc, 0x6000, v82
	v_mfma_f32_16x16x32_f16 v[90:93], v[6:9], v[78:81], v[30:33]
	s_nop 0
	v_addc_co_u32_e32 v83, vcc, 0, v83, vcc
	global_load_dwordx4 v[10:13], v[26:27], off
	s_waitcnt lgkmcnt(1)
	v_mfma_f32_16x16x32_f16 v[54:57], v[14:17], v[22:25], v[54:57]
	v_mfma_f32_16x16x32_f16 v[70:73], v[14:17], v[62:65], v[70:73]
	v_mfma_f32_16x16x32_f16 v[98:101], v[14:17], v[78:81], v[42:45]
	global_load_dwordx4 v[18:21], v[82:83], off
	global_load_dwordx4 v[14:17], v[102:103], off offset:1024
	global_load_dwordx4 v[6:9], v[26:27], off offset:1024
	s_waitcnt lgkmcnt(0)
	v_mfma_f32_16x16x32_f16 v[26:29], v[94:97], v[22:25], v[58:61]
	v_bitop3_b32 v22, v1, v84, 24 bitop3:0x36
	v_lshl_or_b32 v102, v22, 4, v104
	ds_read_b128 v[42:45], v102
	ds_read_b128 v[58:61], v102 offset:8192
	global_load_dwordx4 v[22:25], v[82:83], off offset:1024
	v_mfma_f32_16x16x32_f16 v[30:33], v[94:97], v[62:65], v[66:69]
	v_lshl_or_b32 v62, v85, 4, v84
	v_ashrrev_i32_e32 v63, 31, v62
	v_lshlrev_b64 v[118:119], 2, v[62:63]
	v_lshl_add_u64 v[66:67], s[14:15], 0, v[118:119]
	s_waitcnt vmcnt(5) lgkmcnt(1)
	v_mfma_f32_16x16x32_f16 v[62:65], v[42:45], v[2:5], v[34:37]
	s_nop 2
	global_load_dword v34, v[66:67], off
	v_bitop3_b32 v35, v1, v84, 28 bitop3:0x36
	v_lshl_or_b32 v35, v35, 4, v104
	s_waitcnt vmcnt(5)
	v_mfma_f32_16x16x32_f16 v[46:49], v[42:45], v[10:13], v[46:49]
	v_lshlrev_b32_e32 v1, 5, v1
	s_waitcnt vmcnt(4)
	v_mfma_f32_16x16x32_f16 v[42:45], v[42:45], v[18:21], v[74:77]
	v_mfma_f32_16x16x32_f16 v[50:53], v[94:97], v[78:81], v[50:53]
	ds_read_b128 v[66:69], v35
	ds_read_b128 v[78:81], v102 offset:16384
	ds_read_b128 v[82:85], v102 offset:24576
	ds_read_b128 v[74:77], v35 offset:8192
	ds_read_b128 v[94:97], v35 offset:16384
	ds_read_b128 v[102:105], v35 offset:24576
	ds_read_b128 v[106:109], v1 offset:39936
	ds_read_b128 v[110:113], v1 offset:39952
	s_waitcnt vmcnt(1) lgkmcnt(7)
	v_mfma_f32_16x16x32_f16 v[114:117], v[66:69], v[22:25], v[42:45]
	v_mfma_f32_16x16x32_f16 v[46:49], v[66:69], v[6:9], v[46:49]
	s_waitcnt lgkmcnt(1)
	s_nop 5
	v_mul_f32_e32 v35, v107, v114
	v_mfma_f32_16x16x32_f16 v[62:65], v[66:69], v[14:17], v[62:65]
	v_mfma_f32_16x16x32_f16 v[38:41], v[58:61], v[10:13], v[38:41]
	v_fmac_f32_e32 v35, v106, v46
	s_waitcnt vmcnt(0)
	v_add_f32_e32 v35, v34, v35
	s_nop 3
	v_add_f32_e32 v43, v62, v35
	v_mul_f32_e32 v35, v109, v115
	v_fmac_f32_e32 v35, v108, v47
	v_add_f32_e32 v35, v34, v35
	v_add_f32_e32 v42, v63, v35
	s_waitcnt lgkmcnt(0)
	v_mul_f32_e32 v35, v111, v116
	v_fmac_f32_e32 v35, v110, v48
	v_mfma_f32_16x16x32_f16 v[44:47], v[58:61], v[2:5], v[86:89]
	v_add_f32_e32 v35, v34, v35
	v_add_f32_e32 v37, v64, v35
	v_mul_f32_e32 v35, v113, v117
	v_mfma_f32_16x16x32_f16 v[58:61], v[58:61], v[18:21], v[90:93]
	v_fmac_f32_e32 v35, v112, v49
	v_add_f32_e32 v35, v34, v35
	v_mfma_f32_16x16x32_f16 v[66:69], v[74:77], v[6:9], v[38:41]
	s_nop 2
	v_add_f32_e32 v38, v65, v35
	ds_read_b128 v[62:65], v1 offset:40064
	ds_read_b128 v[86:89], v1 offset:40080
	v_mfma_f32_16x16x32_f16 v[58:61], v[74:77], v[22:25], v[58:61]
	v_mfma_f32_16x16x32_f16 v[44:47], v[74:77], v[14:17], v[44:47]
	v_mfma_f32_16x16x32_f16 v[54:57], v[78:81], v[2:5], v[54:57]
	s_waitcnt lgkmcnt(1)
	s_nop 4
	v_mul_f32_e32 v35, v63, v58
	v_fmac_f32_e32 v35, v62, v66
	v_add_f32_e32 v35, v34, v35
	v_add_f32_e32 v39, v44, v35
	v_mul_f32_e32 v35, v65, v59
	v_fmac_f32_e32 v35, v64, v67
	v_add_f32_e32 v35, v34, v35
	v_add_f32_e32 v40, v45, v35
	s_waitcnt lgkmcnt(0)
	v_mul_f32_e32 v35, v87, v60
	v_fmac_f32_e32 v35, v86, v68
	v_mfma_f32_16x16x32_f16 v[62:65], v[78:81], v[10:13], v[70:73]
	v_add_f32_e32 v35, v34, v35
	v_add_f32_e32 v41, v46, v35
	v_mul_f32_e32 v35, v89, v61
	v_mfma_f32_16x16x32_f16 v[70:73], v[78:81], v[18:21], v[98:101]
	v_fmac_f32_e32 v35, v88, v69
	v_add_f32_e32 v35, v34, v35
	v_add_f32_e32 v36, v47, v35
	v_mfma_f32_16x16x32_f16 v[58:61], v[94:97], v[6:9], v[62:65]
	ds_read_b128 v[44:47], v1 offset:40192
	s_nop 1
	ds_read_b128 v[62:65], v1 offset:40208
	v_mfma_f32_16x16x32_f16 v[66:69], v[94:97], v[22:25], v[70:73]
	v_mfma_f32_16x16x32_f16 v[54:57], v[94:97], v[14:17], v[54:57]
	s_waitcnt lgkmcnt(1)
	s_nop 5
	v_mul_f32_e32 v35, v45, v66
	v_mul_f32_e32 v48, v47, v67
	v_fmac_f32_e32 v35, v44, v58
	v_fmac_f32_e32 v48, v46, v59
	v_mfma_f32_16x16x32_f16 v[44:47], v[82:85], v[2:5], v[26:29]
	v_add_f32_e32 v2, v34, v48
	v_add_f32_e32 v35, v34, v35
	v_add_f32_e32 v35, v54, v35
	s_waitcnt lgkmcnt(0)
	v_mul_f32_e32 v27, v63, v68
	v_fmac_f32_e32 v27, v62, v60
	v_add_f32_e32 v26, v55, v2
	v_mfma_f32_16x16x32_f16 v[2:5], v[82:85], v[10:13], v[30:33]
	v_add_f32_e32 v10, v34, v27
	v_add_f32_e32 v27, v56, v10
	v_mfma_f32_16x16x32_f16 v[10:13], v[82:85], v[18:21], v[50:53]
	v_mul_f32_e32 v18, v65, v69
	v_fmac_f32_e32 v18, v64, v61
	v_add_f32_e32 v18, v34, v18
	v_mfma_f32_16x16x32_f16 v[2:5], v[102:105], v[6:9], v[2:5]
	ds_read_b128 v[28:31], v1 offset:40320
	ds_read_b128 v[6:9], v1 offset:40336
	v_add_f32_e32 v18, v57, v18
	v_mfma_f32_16x16x32_f16 v[10:13], v[102:105], v[22:25], v[10:13]
	v_mfma_f32_16x16x32_f16 v[14:17], v[102:105], v[14:17], v[44:47]
	s_waitcnt lgkmcnt(1)
	s_nop 5
	v_mul_f32_e32 v1, v29, v10
	v_fmac_f32_e32 v1, v28, v2
	v_add_f32_e32 v1, v34, v1
	v_add_f32_e32 v14, v14, v1
	v_mul_f32_e32 v1, v31, v11
	v_fmac_f32_e32 v1, v30, v3
	v_and_b32_e32 v11, 48, v0
	v_add_f32_e32 v1, v34, v1
	ds_read_b32 v2, v11 offset:40448
	v_add_f32_e32 v10, v15, v1
	s_waitcnt lgkmcnt(1)
	v_mul_f32_e32 v1, v7, v12
	v_fmac_f32_e32 v1, v6, v4
	v_add_f32_e32 v0, v34, v1
	v_add_f32_e32 v4, v16, v0
	v_lshl_add_u64 v[0:1], s[22:23], 0, v[118:119]
	s_cbranch_scc1 .LBB3_68
	s_waitcnt lgkmcnt(0)
	v_cmp_lt_i32_e32 vcc, -1, v2
	s_and_saveexec_b64 s[0:1], vcc
	s_cbranch_execz .LBB3_37
	v_mov_b32_e32 v3, 0
	v_lshlrev_b64 v[6:7], 8, v[2:3]
	v_lshl_add_u64 v[6:7], v[0:1], 0, v[6:7]
	global_store_dword v[6:7], v43, off
